# speedup vs baseline: 1.0062x; 1.0062x over previous
.Lu0_1:
	ds_read_b64_tr_b16 v[178:179], v206 offset:24576
	ds_read_b64_tr_b16 v[180:181], v206 offset:25600
	s_waitcnt lgkmcnt(9)
	v_mfma_f32_32x32x16_f16 v[98:113], v[82:85], v[154:157], v[34:49]
	v_add_f32_e32 v224, v66, v70
	v_add_f32_e32 v225, v67, v71
	v_add_f32_e32 v226, v68, v72
	v_add_f32_e32 v227, v69, v73
	v_cvt_pk_f16_f32 v158, v66, v67
	v_cvt_pk_f16_f32 v159, v68, v69
	ds_read_b64_tr_b16 v[174:175], v207 offset:24576
	ds_read_b64_tr_b16 v[176:177], v207 offset:25600
	s_waitcnt lgkmcnt(10)
	v_mfma_f32_32x32x16_f16 v[82:97], v[170:173], v[154:157], v[34:49]
	v_add_f32_e32 v224, v74, v224
	v_add_f32_e32 v225, v75, v225
	v_add_f32_e32 v226, v76, v226
	v_add_f32_e32 v227, v77, v227
	v_cvt_pk_f16_f32 v160, v70, v71
	v_cvt_pk_f16_f32 v161, v72, v73
	ds_read_b64_tr_b16 v[170:171], v206 offset:26624
	ds_read_b64_tr_b16 v[172:173], v206 offset:27648
	s_waitcnt lgkmcnt(11)
	v_mfma_f32_32x32x16_f16 v[98:113], v[166:169], v[146:149], v[98:113]
	v_add_f32_e32 v224, v78, v224
	v_add_f32_e32 v225, v79, v225
	v_add_f32_e32 v226, v80, v226
	v_add_f32_e32 v227, v81, v227
	v_cvt_pk_f16_f32 v150, v74, v75
	v_cvt_pk_f16_f32 v151, v76, v77
	ds_read_b64_tr_b16 v[74:75], v207 offset:26624
	ds_read_b64_tr_b16 v[76:77], v207 offset:27648
	s_waitcnt lgkmcnt(12)
	v_mfma_f32_32x32x16_f16 v[82:97], v[162:165], v[146:149], v[82:97]
	v_add_f32_e32 v224, v50, v224
	v_add_f32_e32 v225, v51, v225
	v_add_f32_e32 v226, v52, v226
	v_add_f32_e32 v227, v53, v227
	v_cvt_pk_f16_f32 v152, v78, v79
	v_cvt_pk_f16_f32 v153, v80, v81
	ds_read_b64_tr_b16 v[70:71], v206 offset:28672
	ds_read_b64_tr_b16 v[72:73], v206 offset:29696
	s_waitcnt lgkmcnt(13)
	v_mfma_f32_32x32x16_f16 v[98:113], v[126:129], v[138:141], v[98:113]
	v_add_f32_e32 v224, v54, v224
	v_add_f32_e32 v225, v55, v225
	v_add_f32_e32 v226, v56, v226
	v_add_f32_e32 v227, v57, v227
	v_cvt_pk_f16_f32 v142, v50, v51
	v_cvt_pk_f16_f32 v143, v52, v53
	ds_read_b64_tr_b16 v[66:67], v207 offset:28672
	ds_read_b64_tr_b16 v[68:69], v207 offset:29696
	s_waitcnt lgkmcnt(14)
	v_mfma_f32_32x32x16_f16 v[82:97], v[122:125], v[138:141], v[82:97]
	v_add_f32_e32 v224, v58, v224
	v_add_f32_e32 v225, v59, v225
	v_add_f32_e32 v226, v60, v226
	v_add_f32_e32 v227, v61, v227
	v_cvt_pk_f16_f32 v144, v54, v55
	v_cvt_pk_f16_f32 v145, v56, v57
	ds_read_b64_tr_b16 v[54:55], v206 offset:30720
	ds_read_b64_tr_b16 v[56:57], v206 offset:31744
	s_waitcnt lgkmcnt(14)
	v_mfma_f32_32x32x16_f16 v[98:113], v[118:121], v[134:137], v[98:113]
	v_add_f32_e32 v224, v62, v224
	v_add_f32_e32 v225, v63, v225
	v_add_f32_e32 v226, v64, v226
	v_add_f32_e32 v227, v65, v227
	v_cvt_pk_f16_f32 v130, v58, v59
	v_cvt_pk_f16_f32 v131, v60, v61
	ds_read_b64_tr_b16 v[50:51], v207 offset:30720
	ds_read_b64_tr_b16 v[52:53], v207 offset:31744
	v_mfma_f32_32x32x16_f16 v[82:97], v[114:117], v[134:137], v[82:97]
	v_add_f32_e32 v224, v224, v225
	v_add_f32_e32 v226, v226, v227
	v_add_f32_e32 v60, v224, v226
	v_cvt_pk_f16_f32 v132, v62, v63
	v_cvt_pk_f16_f32 v133, v64, v65
	s_setprio 1
	s_add_i32 s26, s42, s36
	s_mov_b32 m0, s26
	s_nop 0
	global_load_lds_dwordx4 v221, s[50:51]
	s_add_i32 s26, s39, s35
	s_mov_b32 m0, s26
	s_nop 0
	global_load_lds_dwordx4 v222, s[52:53]
	v_max_f32_e32 v58, v98, v99
	v_max3_f32 v59, v100, v101, v83
	v_max3_f32 v58, v58, v82, v84
	v_max3_f32 v58, v58, v85, v102
	v_max3_f32 v59, v59, v104, v105
	v_max3_f32 v58, v58, v103, v86
	v_max3_f32 v59, v59, v88, v89
	v_max3_f32 v58, v58, v87, v106
	v_max3_f32 v59, v59, v108, v109
	v_max3_f32 v58, v58, v107, v90
	v_max3_f32 v59, v59, v92, v93
	v_max3_f32 v58, v58, v91, v110
	v_max3_f32 v59, v59, v112, v113
	v_max3_f32 v58, v58, v111, v94
	v_max3_f32 v59, v59, v96, v97
	v_max3_f32 v58, v58, v95, v59
	v_add_f32_e32 v198, v183, v60
	v_cmp_lt_f32_e32 vcc, s41, v58
	s_cmp_lg_u64 vcc, 0
	s_cselect_b64 s[26:27], -1, 0
	s_cbranch_vccnz .Lu0_9
.Lu0_2:
	s_setprio 0
	s_waitcnt lgkmcnt(14)
	v_mfma_f32_32x32x16_f16 v[2:17], v[158:161], v[178:181], v[2:17]
	v_exp_f32_e32 v98, v98
	v_exp_f32_e32 v99, v99
	v_exp_f32_e32 v100, v100
	v_exp_f32_e32 v101, v101
	s_waitcnt lgkmcnt(12)
	v_mfma_f32_32x32x16_f16 v[18:33], v[158:161], v[174:177], v[18:33]
	v_exp_f32_e32 v102, v102
	v_exp_f32_e32 v103, v103
	v_exp_f32_e32 v104, v104
	v_exp_f32_e32 v105, v105
	ds_read_b128 v[58:61], v211 offset:16384
	ds_read_b128 v[114:117], v211 offset:20480
	s_waitcnt lgkmcnt(12)
	v_mfma_f32_32x32x16_f16 v[2:17], v[150:153], v[170:173], v[2:17]
	v_exp_f32_e32 v106, v106
	v_exp_f32_e32 v107, v107
	v_exp_f32_e32 v108, v108
	v_exp_f32_e32 v109, v109
	ds_read_b128 v[182:185], v210 offset:16384
	ds_read_b128 v[174:177], v210 offset:20480
	s_waitcnt lgkmcnt(12)
	v_mfma_f32_32x32x16_f16 v[18:33], v[150:153], v[74:77], v[18:33]
	v_exp_f32_e32 v110, v110
	v_exp_f32_e32 v111, v111
	v_exp_f32_e32 v112, v112
	v_exp_f32_e32 v113, v113
	ds_read_b128 v[178:181], v209 offset:16384
	ds_read_b128 v[166:169], v209 offset:20480
	s_waitcnt lgkmcnt(12)
	v_mfma_f32_32x32x16_f16 v[2:17], v[142:145], v[70:73], v[2:17]
	v_exp_f32_e32 v82, v82
	v_exp_f32_e32 v83, v83
	v_exp_f32_e32 v84, v84
	v_exp_f32_e32 v85, v85
	ds_read_b128 v[170:173], v208 offset:16384
	ds_read_b128 v[162:165], v208 offset:20480
	s_waitcnt lgkmcnt(12)
	v_mfma_f32_32x32x16_f16 v[18:33], v[142:145], v[66:69], v[18:33]
	v_exp_f32_e32 v86, v86
	v_exp_f32_e32 v87, v87
	v_exp_f32_e32 v88, v88
	v_exp_f32_e32 v89, v89
	s_waitcnt lgkmcnt(10)
	v_mfma_f32_32x32x16_f16 v[2:17], v[130:133], v[54:57], v[2:17]
	v_exp_f32_e32 v90, v90
	v_exp_f32_e32 v91, v91
	v_exp_f32_e32 v92, v92
	v_exp_f32_e32 v93, v93
	s_waitcnt lgkmcnt(8)
	v_mfma_f32_32x32x16_f16 v[18:33], v[130:133], v[50:53], v[18:33]
	v_exp_f32_e32 v94, v94
	v_exp_f32_e32 v95, v95
	v_exp_f32_e32 v96, v96
	v_exp_f32_e32 v97, v97
	s_waitcnt vmcnt(2) lgkmcnt(0)
	s_barrier
	s_andn2_b64 vcc, exec, s[26:27]
	s_cbranch_vccnz .Lu0_4
	s_waitcnt lgkmcnt(0)
	v_add_u32_e32 v66, s38, v212
	ds_read_b128 v[50:53], v66 offset:49248
	ds_read_b128 v[54:57], v66 offset:49216
	ds_read_b128 v[62:65], v66 offset:49184
	ds_read_b128 v[66:69], v66 offset:49152
	s_waitcnt lgkmcnt(3)
	v_pk_mul_f32 v[14:15], v[14:15], v[50:51]
	s_waitcnt lgkmcnt(2)
	v_pk_mul_f32 v[10:11], v[10:11], v[54:55]
	s_waitcnt lgkmcnt(1)
	v_pk_mul_f32 v[6:7], v[6:7], v[62:63]
	v_pk_mul_f32 v[16:17], v[16:17], v[52:53]
	v_pk_mul_f32 v[12:13], v[12:13], v[56:57]
	v_pk_mul_f32 v[8:9], v[8:9], v[64:65]
	s_waitcnt lgkmcnt(0)
	v_pk_mul_f32 v[4:5], v[4:5], v[68:69]
	v_pk_mul_f32 v[2:3], v[2:3], v[66:67]
	v_pk_mul_f32 v[30:31], v[30:31], v[50:51]
	v_pk_mul_f32 v[26:27], v[26:27], v[54:55]
	v_pk_mul_f32 v[22:23], v[22:23], v[62:63]
	v_pk_mul_f32 v[32:33], v[32:33], v[52:53]
	v_pk_mul_f32 v[28:29], v[28:29], v[56:57]
	v_pk_mul_f32 v[24:25], v[24:25], v[64:65]
	v_pk_mul_f32 v[20:21], v[20:21], v[68:69]
	v_pk_mul_f32 v[18:19], v[18:19], v[66:67]
.Lu0_4:
	s_add_i32 s26, s39, 0x2000
	s_cmpk_lg_i32 s39, 0x4000
	s_cselect_b32 s43, s26, 0
	ds_read_b64_tr_b16 v[126:127], v206 offset:32768
	ds_read_b64_tr_b16 v[128:129], v206 offset:33792
	s_waitcnt lgkmcnt(9)
	v_mfma_f32_32x32x16_f16 v[66:81], v[58:61], v[154:157], v[34:49]
	v_add_f32_e32 v224, v98, v102
	v_add_f32_e32 v225, v99, v103
	v_add_f32_e32 v226, v100, v104
	v_add_f32_e32 v227, v101, v105
	v_cvt_pk_f16_f32 v158, v98, v99
	v_cvt_pk_f16_f32 v159, v100, v101
	ds_read_b64_tr_b16 v[122:123], v207 offset:32768
	ds_read_b64_tr_b16 v[124:125], v207 offset:33792
	s_waitcnt lgkmcnt(10)
	v_mfma_f32_32x32x16_f16 v[50:65], v[114:117], v[154:157], v[34:49]
	v_add_f32_e32 v224, v106, v224
	v_add_f32_e32 v225, v107, v225
	v_add_f32_e32 v226, v108, v226
	v_add_f32_e32 v227, v109, v227
	v_cvt_pk_f16_f32 v160, v102, v103
	v_cvt_pk_f16_f32 v161, v104, v105
	ds_read_b64_tr_b16 v[118:119], v206 offset:34816
	ds_read_b64_tr_b16 v[120:121], v206 offset:35840
	s_waitcnt lgkmcnt(11)
	v_mfma_f32_32x32x16_f16 v[66:81], v[182:185], v[146:149], v[66:81]
	v_add_f32_e32 v224, v110, v224
	v_add_f32_e32 v225, v111, v225
	v_add_f32_e32 v226, v112, v226
	v_add_f32_e32 v227, v113, v227
	v_cvt_pk_f16_f32 v150, v106, v107
	v_cvt_pk_f16_f32 v151, v108, v109
	ds_read_b64_tr_b16 v[114:115], v207 offset:34816
	ds_read_b64_tr_b16 v[116:117], v207 offset:35840
	s_waitcnt lgkmcnt(12)
	v_mfma_f32_32x32x16_f16 v[50:65], v[174:177], v[146:149], v[50:65]
	v_add_f32_e32 v224, v82, v224
	v_add_f32_e32 v225, v83, v225
	v_add_f32_e32 v226, v84, v226
	v_add_f32_e32 v227, v85, v227
	v_cvt_pk_f16_f32 v152, v110, v111
	v_cvt_pk_f16_f32 v153, v112, v113
	ds_read_b64_tr_b16 v[106:107], v206 offset:36864
	ds_read_b64_tr_b16 v[108:109], v206 offset:37888
	s_waitcnt lgkmcnt(13)
	v_mfma_f32_32x32x16_f16 v[66:81], v[178:181], v[138:141], v[66:81]
	v_add_f32_e32 v224, v86, v224
	v_add_f32_e32 v225, v87, v225
	v_add_f32_e32 v226, v88, v226
	v_add_f32_e32 v227, v89, v227
	v_cvt_pk_f16_f32 v142, v82, v83
	v_cvt_pk_f16_f32 v143, v84, v85
	ds_read_b64_tr_b16 v[102:103], v207 offset:36864
	ds_read_b64_tr_b16 v[104:105], v207 offset:37888
	s_waitcnt lgkmcnt(14)
	v_mfma_f32_32x32x16_f16 v[50:65], v[166:169], v[138:141], v[50:65]
	v_add_f32_e32 v224, v90, v224
	v_add_f32_e32 v225, v91, v225
	v_add_f32_e32 v226, v92, v226
	v_add_f32_e32 v227, v93, v227
	v_cvt_pk_f16_f32 v144, v86, v87
	v_cvt_pk_f16_f32 v145, v88, v89
	ds_read_b64_tr_b16 v[98:99], v206 offset:38912
	ds_read_b64_tr_b16 v[100:101], v206 offset:39936
	s_waitcnt lgkmcnt(14)
	v_mfma_f32_32x32x16_f16 v[66:81], v[170:173], v[134:137], v[66:81]
	v_add_f32_e32 v224, v94, v224
	v_add_f32_e32 v225, v95, v225
	v_add_f32_e32 v226, v96, v226
	v_add_f32_e32 v227, v97, v227
	v_cvt_pk_f16_f32 v130, v90, v91
	v_cvt_pk_f16_f32 v131, v92, v93
	ds_read_b64_tr_b16 v[86:87], v207 offset:38912
	ds_read_b64_tr_b16 v[88:89], v207 offset:39936
	v_mfma_f32_32x32x16_f16 v[50:65], v[162:165], v[134:137], v[50:65]
	v_add_f32_e32 v224, v224, v225
	v_add_f32_e32 v226, v226, v227
	v_add_f32_e32 v84, v224, v226
	v_cvt_pk_f16_f32 v132, v94, v95
	v_cvt_pk_f16_f32 v133, v96, v97
	s_setprio 1
	s_add_u32 s54, s50, 0x2000
	s_addc_u32 s55, s51, 0
	s_add_i32 s26, s39, s36
	s_mov_b32 m0, s26
	s_nop 0
	global_load_lds_dwordx4 v221, s[54:55]
	v_max_f32_e32 v82, v66, v67
	s_nop 1
	v_max3_f32 v83, v68, v69, v51
	v_max3_f32 v82, v82, v50, v52
	v_max3_f32 v82, v82, v53, v70
	v_max3_f32 v83, v83, v72, v73
	v_max3_f32 v82, v82, v71, v54
	v_max3_f32 v83, v83, v56, v57
	v_max3_f32 v82, v82, v55, v74
	v_max3_f32 v83, v83, v76, v77
	v_max3_f32 v82, v82, v75, v58
	v_max3_f32 v83, v83, v60, v61
	v_max3_f32 v82, v82, v59, v78
	v_max3_f32 v83, v83, v80, v81
	v_max3_f32 v82, v82, v79, v62
	v_max3_f32 v83, v83, v64, v65
	v_max3_f32 v82, v82, v63, v83
	v_add_f32_e32 v183, v198, v84
	s_add_u32 s54, s52, 0x2000
	s_addc_u32 s55, s53, 0
	s_add_i32 s26, s43, s35
	s_mov_b32 m0, s26
	s_nop 0
	global_load_lds_dwordx4 v222, s[54:55]
	v_cmp_lt_f32_e32 vcc, s41, v82
	s_cmp_lg_u64 vcc, 0
	s_cselect_b64 s[26:27], -1, 0
	s_cbranch_vccnz .Lu0_12
.Lu0_5:
	s_setprio 0
	s_waitcnt lgkmcnt(14)
	v_mfma_f32_32x32x16_f16 v[2:17], v[158:161], v[126:129], v[2:17]
	v_exp_f32_e32 v66, v66
	v_exp_f32_e32 v67, v67
	v_exp_f32_e32 v68, v68
	v_exp_f32_e32 v69, v69
	s_waitcnt lgkmcnt(12)
	v_mfma_f32_32x32x16_f16 v[18:33], v[158:161], v[122:125], v[18:33]
	v_exp_f32_e32 v70, v70
	v_exp_f32_e32 v71, v71
	v_exp_f32_e32 v72, v72
	v_exp_f32_e32 v73, v73
	ds_read_b128 v[82:85], v211
	ds_read_b128 v[170:173], v211 offset:4096
	s_waitcnt lgkmcnt(12)
	v_mfma_f32_32x32x16_f16 v[2:17], v[150:153], v[118:121], v[2:17]
	v_exp_f32_e32 v74, v74
	v_exp_f32_e32 v75, v75
	v_exp_f32_e32 v76, v76
	v_exp_f32_e32 v77, v77
	ds_read_b128 v[166:169], v210
	ds_read_b128 v[162:165], v210 offset:4096
	s_waitcnt lgkmcnt(12)
	v_mfma_f32_32x32x16_f16 v[18:33], v[150:153], v[114:117], v[18:33]
	v_exp_f32_e32 v78, v78
	v_exp_f32_e32 v79, v79
	v_exp_f32_e32 v80, v80
	v_exp_f32_e32 v81, v81
	ds_read_b128 v[126:129], v209
	ds_read_b128 v[122:125], v209 offset:4096
	s_waitcnt lgkmcnt(12)
	v_mfma_f32_32x32x16_f16 v[2:17], v[142:145], v[106:109], v[2:17]
	v_exp_f32_e32 v50, v50
	v_exp_f32_e32 v51, v51
	v_exp_f32_e32 v52, v52
	v_exp_f32_e32 v53, v53
	ds_read_b128 v[118:121], v208
	ds_read_b128 v[114:117], v208 offset:4096
	s_waitcnt lgkmcnt(12)
	v_mfma_f32_32x32x16_f16 v[18:33], v[142:145], v[102:105], v[18:33]
	v_exp_f32_e32 v54, v54
	v_exp_f32_e32 v55, v55
	v_exp_f32_e32 v56, v56
	v_exp_f32_e32 v57, v57
	s_waitcnt lgkmcnt(10)
	v_mfma_f32_32x32x16_f16 v[2:17], v[130:133], v[98:101], v[2:17]
	v_exp_f32_e32 v58, v58
	v_exp_f32_e32 v59, v59
	v_exp_f32_e32 v60, v60
	v_exp_f32_e32 v61, v61
	s_waitcnt lgkmcnt(8)
	v_mfma_f32_32x32x16_f16 v[18:33], v[130:133], v[86:89], v[18:33]
	v_exp_f32_e32 v62, v62
	v_exp_f32_e32 v63, v63
	v_exp_f32_e32 v64, v64
	v_exp_f32_e32 v65, v65
	s_waitcnt vmcnt(2) lgkmcnt(0)
	s_barrier
	s_andn2_b64 vcc, exec, s[26:27]
	s_cbranch_vccnz .Lu0_7
	s_waitcnt lgkmcnt(0)
	v_add_u32_e32 v98, s38, v212
	ds_read_b128 v[86:89], v98 offset:49248
	ds_read_b128 v[90:93], v98 offset:49216
	ds_read_b128 v[94:97], v98 offset:49152
	ds_read_b128 v[98:101], v98 offset:49184
	s_waitcnt lgkmcnt(3)
	v_pk_mul_f32 v[16:17], v[16:17], v[88:89]
	v_pk_mul_f32 v[14:15], v[14:15], v[86:87]
	s_waitcnt lgkmcnt(2)
	v_pk_mul_f32 v[12:13], v[12:13], v[92:93]
	v_pk_mul_f32 v[10:11], v[10:11], v[90:91]
	s_waitcnt lgkmcnt(0)
	v_pk_mul_f32 v[8:9], v[8:9], v[100:101]
	v_pk_mul_f32 v[6:7], v[6:7], v[98:99]
	v_pk_mul_f32 v[4:5], v[4:5], v[96:97]
	v_pk_mul_f32 v[2:3], v[2:3], v[94:95]
	v_pk_mul_f32 v[32:33], v[32:33], v[88:89]
	v_pk_mul_f32 v[30:31], v[30:31], v[86:87]
	v_pk_mul_f32 v[28:29], v[28:29], v[92:93]
	v_pk_mul_f32 v[26:27], v[26:27], v[90:91]
	v_pk_mul_f32 v[24:25], v[24:25], v[100:101]
	v_pk_mul_f32 v[22:23], v[22:23], v[98:99]
	v_pk_mul_f32 v[20:21], v[20:21], v[96:97]
	v_pk_mul_f32 v[18:19], v[18:19], v[94:95]

.Lu1_1:
	ds_read_b64_tr_b16 v[178:179], v206 offset:40960
	ds_read_b64_tr_b16 v[180:181], v206 offset:41984
	s_waitcnt lgkmcnt(9)
	v_mfma_f32_32x32x16_f16 v[98:113], v[82:85], v[154:157], v[34:49]
	v_add_f32_e32 v224, v66, v70
	v_add_f32_e32 v225, v67, v71
	v_add_f32_e32 v226, v68, v72
	v_add_f32_e32 v227, v69, v73
	v_cvt_pk_f16_f32 v158, v66, v67
	v_cvt_pk_f16_f32 v159, v68, v69
	ds_read_b64_tr_b16 v[174:175], v207 offset:40960
	ds_read_b64_tr_b16 v[176:177], v207 offset:41984
	s_waitcnt lgkmcnt(10)
	v_mfma_f32_32x32x16_f16 v[82:97], v[170:173], v[154:157], v[34:49]
	v_add_f32_e32 v224, v74, v224
	v_add_f32_e32 v225, v75, v225
	v_add_f32_e32 v226, v76, v226
	v_add_f32_e32 v227, v77, v227
	v_cvt_pk_f16_f32 v160, v70, v71
	v_cvt_pk_f16_f32 v161, v72, v73
	ds_read_b64_tr_b16 v[170:171], v206 offset:43008
	ds_read_b64_tr_b16 v[172:173], v206 offset:44032
	s_waitcnt lgkmcnt(11)
	v_mfma_f32_32x32x16_f16 v[98:113], v[166:169], v[146:149], v[98:113]
	v_add_f32_e32 v224, v78, v224
	v_add_f32_e32 v225, v79, v225
	v_add_f32_e32 v226, v80, v226
	v_add_f32_e32 v227, v81, v227
	v_cvt_pk_f16_f32 v150, v74, v75
	v_cvt_pk_f16_f32 v151, v76, v77
	ds_read_b64_tr_b16 v[74:75], v207 offset:43008
	ds_read_b64_tr_b16 v[76:77], v207 offset:44032
	s_waitcnt lgkmcnt(12)
	v_mfma_f32_32x32x16_f16 v[82:97], v[162:165], v[146:149], v[82:97]
	v_add_f32_e32 v224, v50, v224
	v_add_f32_e32 v225, v51, v225
	v_add_f32_e32 v226, v52, v226
	v_add_f32_e32 v227, v53, v227
	v_cvt_pk_f16_f32 v152, v78, v79
	v_cvt_pk_f16_f32 v153, v80, v81
	ds_read_b64_tr_b16 v[70:71], v206 offset:45056
	ds_read_b64_tr_b16 v[72:73], v206 offset:46080
	s_waitcnt lgkmcnt(13)
	v_mfma_f32_32x32x16_f16 v[98:113], v[126:129], v[138:141], v[98:113]
	v_add_f32_e32 v224, v54, v224
	v_add_f32_e32 v225, v55, v225
	v_add_f32_e32 v226, v56, v226
	v_add_f32_e32 v227, v57, v227
	v_cvt_pk_f16_f32 v142, v50, v51
	v_cvt_pk_f16_f32 v143, v52, v53
	ds_read_b64_tr_b16 v[66:67], v207 offset:45056
	ds_read_b64_tr_b16 v[68:69], v207 offset:46080
	s_waitcnt lgkmcnt(14)
	v_mfma_f32_32x32x16_f16 v[82:97], v[122:125], v[138:141], v[82:97]
	v_add_f32_e32 v224, v58, v224
	v_add_f32_e32 v225, v59, v225
	v_add_f32_e32 v226, v60, v226
	v_add_f32_e32 v227, v61, v227
	v_cvt_pk_f16_f32 v144, v54, v55
	v_cvt_pk_f16_f32 v145, v56, v57
	ds_read_b64_tr_b16 v[54:55], v206 offset:47104
	ds_read_b64_tr_b16 v[56:57], v206 offset:48128
	s_waitcnt lgkmcnt(14)
	v_mfma_f32_32x32x16_f16 v[98:113], v[118:121], v[134:137], v[98:113]
	v_add_f32_e32 v224, v62, v224
	v_add_f32_e32 v225, v63, v225
	v_add_f32_e32 v226, v64, v226
	v_add_f32_e32 v227, v65, v227
	v_cvt_pk_f16_f32 v130, v58, v59
	v_cvt_pk_f16_f32 v131, v60, v61
	ds_read_b64_tr_b16 v[50:51], v207 offset:47104
	ds_read_b64_tr_b16 v[52:53], v207 offset:48128
	v_mfma_f32_32x32x16_f16 v[82:97], v[114:117], v[134:137], v[82:97]
	v_add_f32_e32 v224, v224, v225
	v_add_f32_e32 v226, v226, v227
	v_add_f32_e32 v60, v224, v226
	v_cvt_pk_f16_f32 v132, v62, v63
	v_cvt_pk_f16_f32 v133, v64, v65
	s_setprio 1
	s_add_i32 s26, s42, s36
	s_mov_b32 m0, s26
	s_nop 0
	global_load_lds_dwordx4 v221, s[50:51]
	s_add_i32 s26, s39, s35
	s_mov_b32 m0, s26
	s_nop 0
	global_load_lds_dwordx4 v222, s[52:53]
	v_max_f32_e32 v58, v98, v99
	v_max3_f32 v59, v100, v101, v83
	v_max3_f32 v58, v58, v82, v84
	v_max3_f32 v58, v58, v85, v102
	v_max3_f32 v59, v59, v104, v105
	v_max3_f32 v58, v58, v103, v86
	v_max3_f32 v59, v59, v88, v89
	v_max3_f32 v58, v58, v87, v106
	v_max3_f32 v59, v59, v108, v109
	v_max3_f32 v58, v58, v107, v90
	v_max3_f32 v59, v59, v92, v93
	v_max3_f32 v58, v58, v91, v110
	v_max3_f32 v59, v59, v112, v113
	v_max3_f32 v58, v58, v111, v94
	v_max3_f32 v59, v59, v96, v97
	v_max3_f32 v58, v58, v95, v59
	v_add_f32_e32 v198, v183, v60
	v_cmp_lt_f32_e32 vcc, s41, v58
	s_cmp_lg_u64 vcc, 0
	s_cselect_b64 s[26:27], -1, 0
	s_cbranch_vccnz .Lu1_9
.Lu1_2:
	s_setprio 0
	s_waitcnt lgkmcnt(14)
	v_mfma_f32_32x32x16_f16 v[2:17], v[158:161], v[178:181], v[2:17]
	v_exp_f32_e32 v98, v98
	v_exp_f32_e32 v99, v99
	v_exp_f32_e32 v100, v100
	v_exp_f32_e32 v101, v101
	s_waitcnt lgkmcnt(12)
	v_mfma_f32_32x32x16_f16 v[18:33], v[158:161], v[174:177], v[18:33]
	v_exp_f32_e32 v102, v102
	v_exp_f32_e32 v103, v103
	v_exp_f32_e32 v104, v104
	v_exp_f32_e32 v105, v105
	ds_read_b128 v[58:61], v211 offset:8192
	ds_read_b128 v[114:117], v211 offset:12288
	s_waitcnt lgkmcnt(12)
	v_mfma_f32_32x32x16_f16 v[2:17], v[150:153], v[170:173], v[2:17]
	v_exp_f32_e32 v106, v106
	v_exp_f32_e32 v107, v107
	v_exp_f32_e32 v108, v108
	v_exp_f32_e32 v109, v109
	ds_read_b128 v[182:185], v210 offset:8192
	ds_read_b128 v[174:177], v210 offset:12288
	s_waitcnt lgkmcnt(12)
	v_mfma_f32_32x32x16_f16 v[18:33], v[150:153], v[74:77], v[18:33]
	v_exp_f32_e32 v110, v110
	v_exp_f32_e32 v111, v111
	v_exp_f32_e32 v112, v112
	v_exp_f32_e32 v113, v113
	ds_read_b128 v[178:181], v209 offset:8192
	ds_read_b128 v[166:169], v209 offset:12288
	s_waitcnt lgkmcnt(12)
	v_mfma_f32_32x32x16_f16 v[2:17], v[142:145], v[70:73], v[2:17]
	v_exp_f32_e32 v82, v82
	v_exp_f32_e32 v83, v83
	v_exp_f32_e32 v84, v84
	v_exp_f32_e32 v85, v85
	ds_read_b128 v[170:173], v208 offset:8192
	ds_read_b128 v[162:165], v208 offset:12288
	s_waitcnt lgkmcnt(12)
	v_mfma_f32_32x32x16_f16 v[18:33], v[142:145], v[66:69], v[18:33]
	v_exp_f32_e32 v86, v86
	v_exp_f32_e32 v87, v87
	v_exp_f32_e32 v88, v88
	v_exp_f32_e32 v89, v89
	s_waitcnt lgkmcnt(10)
	v_mfma_f32_32x32x16_f16 v[2:17], v[130:133], v[54:57], v[2:17]
	v_exp_f32_e32 v90, v90
	v_exp_f32_e32 v91, v91
	v_exp_f32_e32 v92, v92
	v_exp_f32_e32 v93, v93
	s_waitcnt lgkmcnt(8)
	v_mfma_f32_32x32x16_f16 v[18:33], v[130:133], v[50:53], v[18:33]
	v_exp_f32_e32 v94, v94
	v_exp_f32_e32 v95, v95
	v_exp_f32_e32 v96, v96
	v_exp_f32_e32 v97, v97
	s_waitcnt vmcnt(2) lgkmcnt(0)
	s_barrier
	s_andn2_b64 vcc, exec, s[26:27]
	s_cbranch_vccnz .Lu1_4
	s_waitcnt lgkmcnt(0)
	v_add_u32_e32 v66, s38, v212
	ds_read_b128 v[50:53], v66 offset:49248
	ds_read_b128 v[54:57], v66 offset:49216
	ds_read_b128 v[62:65], v66 offset:49184
	ds_read_b128 v[66:69], v66 offset:49152
	s_waitcnt lgkmcnt(3)
	v_pk_mul_f32 v[14:15], v[14:15], v[50:51]
	s_waitcnt lgkmcnt(2)
	v_pk_mul_f32 v[10:11], v[10:11], v[54:55]
	s_waitcnt lgkmcnt(1)
	v_pk_mul_f32 v[6:7], v[6:7], v[62:63]
	v_pk_mul_f32 v[16:17], v[16:17], v[52:53]
	v_pk_mul_f32 v[12:13], v[12:13], v[56:57]
	v_pk_mul_f32 v[8:9], v[8:9], v[64:65]
	s_waitcnt lgkmcnt(0)
	v_pk_mul_f32 v[4:5], v[4:5], v[68:69]
	v_pk_mul_f32 v[2:3], v[2:3], v[66:67]
	v_pk_mul_f32 v[30:31], v[30:31], v[50:51]
	v_pk_mul_f32 v[26:27], v[26:27], v[54:55]
	v_pk_mul_f32 v[22:23], v[22:23], v[62:63]
	v_pk_mul_f32 v[32:33], v[32:33], v[52:53]
	v_pk_mul_f32 v[28:29], v[28:29], v[56:57]
	v_pk_mul_f32 v[24:25], v[24:25], v[64:65]
	v_pk_mul_f32 v[20:21], v[20:21], v[68:69]
	v_pk_mul_f32 v[18:19], v[18:19], v[66:67]
.Lu1_4:
	s_add_i32 s26, s39, 0x2000
	s_cmpk_lg_i32 s39, 0x4000
	s_cselect_b32 s43, s26, 0
	ds_read_b64_tr_b16 v[126:127], v206 offset:24576
	ds_read_b64_tr_b16 v[128:129], v206 offset:25600
	s_waitcnt lgkmcnt(9)
	v_mfma_f32_32x32x16_f16 v[66:81], v[58:61], v[154:157], v[34:49]
	v_add_f32_e32 v224, v98, v102
	v_add_f32_e32 v225, v99, v103
	v_add_f32_e32 v226, v100, v104
	v_add_f32_e32 v227, v101, v105
	v_cvt_pk_f16_f32 v158, v98, v99
	v_cvt_pk_f16_f32 v159, v100, v101
	ds_read_b64_tr_b16 v[122:123], v207 offset:24576
	ds_read_b64_tr_b16 v[124:125], v207 offset:25600
	s_waitcnt lgkmcnt(10)
	v_mfma_f32_32x32x16_f16 v[50:65], v[114:117], v[154:157], v[34:49]
	v_add_f32_e32 v224, v106, v224
	v_add_f32_e32 v225, v107, v225
	v_add_f32_e32 v226, v108, v226
	v_add_f32_e32 v227, v109, v227
	v_cvt_pk_f16_f32 v160, v102, v103
	v_cvt_pk_f16_f32 v161, v104, v105
	ds_read_b64_tr_b16 v[118:119], v206 offset:26624
	ds_read_b64_tr_b16 v[120:121], v206 offset:27648
	s_waitcnt lgkmcnt(11)
	v_mfma_f32_32x32x16_f16 v[66:81], v[182:185], v[146:149], v[66:81]
	v_add_f32_e32 v224, v110, v224
	v_add_f32_e32 v225, v111, v225
	v_add_f32_e32 v226, v112, v226
	v_add_f32_e32 v227, v113, v227
	v_cvt_pk_f16_f32 v150, v106, v107
	v_cvt_pk_f16_f32 v151, v108, v109
	ds_read_b64_tr_b16 v[114:115], v207 offset:26624
	ds_read_b64_tr_b16 v[116:117], v207 offset:27648
	s_waitcnt lgkmcnt(12)
	v_mfma_f32_32x32x16_f16 v[50:65], v[174:177], v[146:149], v[50:65]
	v_add_f32_e32 v224, v82, v224
	v_add_f32_e32 v225, v83, v225
	v_add_f32_e32 v226, v84, v226
	v_add_f32_e32 v227, v85, v227
	v_cvt_pk_f16_f32 v152, v110, v111
	v_cvt_pk_f16_f32 v153, v112, v113
	ds_read_b64_tr_b16 v[106:107], v206 offset:28672
	ds_read_b64_tr_b16 v[108:109], v206 offset:29696
	s_waitcnt lgkmcnt(13)
	v_mfma_f32_32x32x16_f16 v[66:81], v[178:181], v[138:141], v[66:81]
	v_add_f32_e32 v224, v86, v224
	v_add_f32_e32 v225, v87, v225
	v_add_f32_e32 v226, v88, v226
	v_add_f32_e32 v227, v89, v227
	v_cvt_pk_f16_f32 v142, v82, v83
	v_cvt_pk_f16_f32 v143, v84, v85
	ds_read_b64_tr_b16 v[102:103], v207 offset:28672
	ds_read_b64_tr_b16 v[104:105], v207 offset:29696
	s_waitcnt lgkmcnt(14)
	v_mfma_f32_32x32x16_f16 v[50:65], v[166:169], v[138:141], v[50:65]
	v_add_f32_e32 v224, v90, v224
	v_add_f32_e32 v225, v91, v225
	v_add_f32_e32 v226, v92, v226
	v_add_f32_e32 v227, v93, v227
	v_cvt_pk_f16_f32 v144, v86, v87
	v_cvt_pk_f16_f32 v145, v88, v89
	ds_read_b64_tr_b16 v[98:99], v206 offset:30720
	ds_read_b64_tr_b16 v[100:101], v206 offset:31744
	s_waitcnt lgkmcnt(14)
	v_mfma_f32_32x32x16_f16 v[66:81], v[170:173], v[134:137], v[66:81]
	v_add_f32_e32 v224, v94, v224
	v_add_f32_e32 v225, v95, v225
	v_add_f32_e32 v226, v96, v226
	v_add_f32_e32 v227, v97, v227
	v_cvt_pk_f16_f32 v130, v90, v91
	v_cvt_pk_f16_f32 v131, v92, v93
	ds_read_b64_tr_b16 v[86:87], v207 offset:30720
	ds_read_b64_tr_b16 v[88:89], v207 offset:31744
	v_mfma_f32_32x32x16_f16 v[50:65], v[162:165], v[134:137], v[50:65]
	v_add_f32_e32 v224, v224, v225
	v_add_f32_e32 v226, v226, v227
	v_add_f32_e32 v84, v224, v226
	v_cvt_pk_f16_f32 v132, v94, v95
	v_cvt_pk_f16_f32 v133, v96, v97
	s_setprio 1
	s_add_u32 s54, s50, 0x2000
	s_addc_u32 s55, s51, 0
	s_add_i32 s26, s39, s36
	s_mov_b32 m0, s26
	s_nop 0
	global_load_lds_dwordx4 v221, s[54:55]
	v_max_f32_e32 v82, v66, v67
	s_nop 1
	v_max3_f32 v83, v68, v69, v51
	v_max3_f32 v82, v82, v50, v52
	v_max3_f32 v82, v82, v53, v70
	v_max3_f32 v83, v83, v72, v73
	v_max3_f32 v82, v82, v71, v54
	v_max3_f32 v83, v83, v56, v57
	v_max3_f32 v82, v82, v55, v74
	v_max3_f32 v83, v83, v76, v77
	v_max3_f32 v82, v82, v75, v58
	v_max3_f32 v83, v83, v60, v61
	v_max3_f32 v82, v82, v59, v78
	v_max3_f32 v83, v83, v80, v81
	v_max3_f32 v82, v82, v79, v62
	v_max3_f32 v83, v83, v64, v65
	v_max3_f32 v82, v82, v63, v83
	v_add_f32_e32 v183, v198, v84
	s_add_u32 s54, s52, 0x2000
	s_addc_u32 s55, s53, 0
	s_add_i32 s26, s43, s35
	s_mov_b32 m0, s26
	s_nop 0
	global_load_lds_dwordx4 v222, s[54:55]
	v_cmp_lt_f32_e32 vcc, s41, v82
	s_cmp_lg_u64 vcc, 0
	s_cselect_b64 s[26:27], -1, 0
	s_cbranch_vccnz .Lu1_12
.Lu1_5:
	s_setprio 0
	s_waitcnt lgkmcnt(14)
	v_mfma_f32_32x32x16_f16 v[2:17], v[158:161], v[126:129], v[2:17]
	v_exp_f32_e32 v66, v66
	v_exp_f32_e32 v67, v67
	v_exp_f32_e32 v68, v68
	v_exp_f32_e32 v69, v69
	s_waitcnt lgkmcnt(12)
	v_mfma_f32_32x32x16_f16 v[18:33], v[158:161], v[122:125], v[18:33]
	v_exp_f32_e32 v70, v70
	v_exp_f32_e32 v71, v71
	v_exp_f32_e32 v72, v72
	v_exp_f32_e32 v73, v73
	ds_read_b128 v[82:85], v211 offset:16384
	ds_read_b128 v[170:173], v211 offset:20480
	s_waitcnt lgkmcnt(12)
	v_mfma_f32_32x32x16_f16 v[2:17], v[150:153], v[118:121], v[2:17]
	v_exp_f32_e32 v74, v74
	v_exp_f32_e32 v75, v75
	v_exp_f32_e32 v76, v76
	v_exp_f32_e32 v77, v77
	ds_read_b128 v[166:169], v210 offset:16384
	ds_read_b128 v[162:165], v210 offset:20480
	s_waitcnt lgkmcnt(12)
	v_mfma_f32_32x32x16_f16 v[18:33], v[150:153], v[114:117], v[18:33]
	v_exp_f32_e32 v78, v78
	v_exp_f32_e32 v79, v79
	v_exp_f32_e32 v80, v80
	v_exp_f32_e32 v81, v81
	ds_read_b128 v[126:129], v209 offset:16384
	ds_read_b128 v[122:125], v209 offset:20480
	s_waitcnt lgkmcnt(12)
	v_mfma_f32_32x32x16_f16 v[2:17], v[142:145], v[106:109], v[2:17]
	v_exp_f32_e32 v50, v50
	v_exp_f32_e32 v51, v51
	v_exp_f32_e32 v52, v52
	v_exp_f32_e32 v53, v53
	ds_read_b128 v[118:121], v208 offset:16384
	ds_read_b128 v[114:117], v208 offset:20480
	s_waitcnt lgkmcnt(12)
	v_mfma_f32_32x32x16_f16 v[18:33], v[142:145], v[102:105], v[18:33]
	v_exp_f32_e32 v54, v54
	v_exp_f32_e32 v55, v55
	v_exp_f32_e32 v56, v56
	v_exp_f32_e32 v57, v57
	s_waitcnt lgkmcnt(10)
	v_mfma_f32_32x32x16_f16 v[2:17], v[130:133], v[98:101], v[2:17]
	v_exp_f32_e32 v58, v58
	v_exp_f32_e32 v59, v59
	v_exp_f32_e32 v60, v60
	v_exp_f32_e32 v61, v61
	s_waitcnt lgkmcnt(8)
	v_mfma_f32_32x32x16_f16 v[18:33], v[130:133], v[86:89], v[18:33]
	v_exp_f32_e32 v62, v62
	v_exp_f32_e32 v63, v63
	v_exp_f32_e32 v64, v64
	v_exp_f32_e32 v65, v65
	s_waitcnt vmcnt(2) lgkmcnt(0)
	s_barrier
	s_andn2_b64 vcc, exec, s[26:27]
	s_cbranch_vccnz .Lu1_7
	s_waitcnt lgkmcnt(0)
	v_add_u32_e32 v98, s38, v212
	ds_read_b128 v[86:89], v98 offset:49248
	ds_read_b128 v[90:93], v98 offset:49216
	ds_read_b128 v[94:97], v98 offset:49152
	ds_read_b128 v[98:101], v98 offset:49184
	s_waitcnt lgkmcnt(3)
	v_pk_mul_f32 v[16:17], v[16:17], v[88:89]
	v_pk_mul_f32 v[14:15], v[14:15], v[86:87]
	s_waitcnt lgkmcnt(2)
	v_pk_mul_f32 v[12:13], v[12:13], v[92:93]
	v_pk_mul_f32 v[10:11], v[10:11], v[90:91]
	s_waitcnt lgkmcnt(0)
	v_pk_mul_f32 v[8:9], v[8:9], v[100:101]
	v_pk_mul_f32 v[6:7], v[6:7], v[98:99]
	v_pk_mul_f32 v[4:5], v[4:5], v[96:97]
	v_pk_mul_f32 v[2:3], v[2:3], v[94:95]
	v_pk_mul_f32 v[32:33], v[32:33], v[88:89]
	v_pk_mul_f32 v[30:31], v[30:31], v[86:87]
	v_pk_mul_f32 v[28:29], v[28:29], v[92:93]
	v_pk_mul_f32 v[26:27], v[26:27], v[90:91]
	v_pk_mul_f32 v[24:25], v[24:25], v[100:101]
	v_pk_mul_f32 v[22:23], v[22:23], v[98:99]
	v_pk_mul_f32 v[20:21], v[20:21], v[96:97]
	v_pk_mul_f32 v[18:19], v[18:19], v[94:95]

.Lu2_1:
	ds_read_b64_tr_b16 v[178:179], v206 offset:32768
	ds_read_b64_tr_b16 v[180:181], v206 offset:33792
	s_waitcnt lgkmcnt(9)
	v_mfma_f32_32x32x16_f16 v[98:113], v[82:85], v[154:157], v[34:49]
	v_add_f32_e32 v224, v66, v70
	v_add_f32_e32 v225, v67, v71
	v_add_f32_e32 v226, v68, v72
	v_add_f32_e32 v227, v69, v73
	v_cvt_pk_f16_f32 v158, v66, v67
	v_cvt_pk_f16_f32 v159, v68, v69
	ds_read_b64_tr_b16 v[174:175], v207 offset:32768
	ds_read_b64_tr_b16 v[176:177], v207 offset:33792
	s_waitcnt lgkmcnt(10)
	v_mfma_f32_32x32x16_f16 v[82:97], v[170:173], v[154:157], v[34:49]
	v_add_f32_e32 v224, v74, v224
	v_add_f32_e32 v225, v75, v225
	v_add_f32_e32 v226, v76, v226
	v_add_f32_e32 v227, v77, v227
	v_cvt_pk_f16_f32 v160, v70, v71
	v_cvt_pk_f16_f32 v161, v72, v73
	ds_read_b64_tr_b16 v[170:171], v206 offset:34816
	ds_read_b64_tr_b16 v[172:173], v206 offset:35840
	s_waitcnt lgkmcnt(11)
	v_mfma_f32_32x32x16_f16 v[98:113], v[166:169], v[146:149], v[98:113]
	v_add_f32_e32 v224, v78, v224
	v_add_f32_e32 v225, v79, v225
	v_add_f32_e32 v226, v80, v226
	v_add_f32_e32 v227, v81, v227
	v_cvt_pk_f16_f32 v150, v74, v75
	v_cvt_pk_f16_f32 v151, v76, v77
	ds_read_b64_tr_b16 v[74:75], v207 offset:34816
	ds_read_b64_tr_b16 v[76:77], v207 offset:35840
	s_waitcnt lgkmcnt(12)
	v_mfma_f32_32x32x16_f16 v[82:97], v[162:165], v[146:149], v[82:97]
	v_add_f32_e32 v224, v50, v224
	v_add_f32_e32 v225, v51, v225
	v_add_f32_e32 v226, v52, v226
	v_add_f32_e32 v227, v53, v227
	v_cvt_pk_f16_f32 v152, v78, v79
	v_cvt_pk_f16_f32 v153, v80, v81
	ds_read_b64_tr_b16 v[70:71], v206 offset:36864
	ds_read_b64_tr_b16 v[72:73], v206 offset:37888
	s_waitcnt lgkmcnt(13)
	v_mfma_f32_32x32x16_f16 v[98:113], v[126:129], v[138:141], v[98:113]
	v_add_f32_e32 v224, v54, v224
	v_add_f32_e32 v225, v55, v225
	v_add_f32_e32 v226, v56, v226
	v_add_f32_e32 v227, v57, v227
	v_cvt_pk_f16_f32 v142, v50, v51
	v_cvt_pk_f16_f32 v143, v52, v53
	ds_read_b64_tr_b16 v[66:67], v207 offset:36864
	ds_read_b64_tr_b16 v[68:69], v207 offset:37888
	s_waitcnt lgkmcnt(14)
	v_mfma_f32_32x32x16_f16 v[82:97], v[122:125], v[138:141], v[82:97]
	v_add_f32_e32 v224, v58, v224
	v_add_f32_e32 v225, v59, v225
	v_add_f32_e32 v226, v60, v226
	v_add_f32_e32 v227, v61, v227
	v_cvt_pk_f16_f32 v144, v54, v55
	v_cvt_pk_f16_f32 v145, v56, v57
	ds_read_b64_tr_b16 v[54:55], v206 offset:38912
	ds_read_b64_tr_b16 v[56:57], v206 offset:39936
	s_waitcnt lgkmcnt(14)
	v_mfma_f32_32x32x16_f16 v[98:113], v[118:121], v[134:137], v[98:113]
	v_add_f32_e32 v224, v62, v224
	v_add_f32_e32 v225, v63, v225
	v_add_f32_e32 v226, v64, v226
	v_add_f32_e32 v227, v65, v227
	v_cvt_pk_f16_f32 v130, v58, v59
	v_cvt_pk_f16_f32 v131, v60, v61
	ds_read_b64_tr_b16 v[50:51], v207 offset:38912
	ds_read_b64_tr_b16 v[52:53], v207 offset:39936
	v_mfma_f32_32x32x16_f16 v[82:97], v[114:117], v[134:137], v[82:97]
	v_add_f32_e32 v224, v224, v225
	v_add_f32_e32 v226, v226, v227
	v_add_f32_e32 v60, v224, v226
	v_cvt_pk_f16_f32 v132, v62, v63
	v_cvt_pk_f16_f32 v133, v64, v65
	s_setprio 1
	s_add_i32 s26, s42, s36
	s_mov_b32 m0, s26
	s_nop 0
	global_load_lds_dwordx4 v221, s[50:51]
	s_add_i32 s26, s39, s35
	s_mov_b32 m0, s26
	s_nop 0
	global_load_lds_dwordx4 v222, s[52:53]
	v_max_f32_e32 v58, v98, v99
	v_max3_f32 v59, v100, v101, v83
	v_max3_f32 v58, v58, v82, v84
	v_max3_f32 v58, v58, v85, v102
	v_max3_f32 v59, v59, v104, v105
	v_max3_f32 v58, v58, v103, v86
	v_max3_f32 v59, v59, v88, v89
	v_max3_f32 v58, v58, v87, v106
	v_max3_f32 v59, v59, v108, v109
	v_max3_f32 v58, v58, v107, v90
	v_max3_f32 v59, v59, v92, v93
	v_max3_f32 v58, v58, v91, v110
	v_max3_f32 v59, v59, v112, v113
	v_max3_f32 v58, v58, v111, v94
	v_max3_f32 v59, v59, v96, v97
	v_max3_f32 v58, v58, v95, v59
	v_add_f32_e32 v198, v183, v60
	v_cmp_lt_f32_e32 vcc, s41, v58
	s_cmp_lg_u64 vcc, 0
	s_cselect_b64 s[26:27], -1, 0
	s_cbranch_vccnz .Lu2_9
.Lu2_2:
	s_setprio 0
	s_waitcnt lgkmcnt(14)
	v_mfma_f32_32x32x16_f16 v[2:17], v[158:161], v[178:181], v[2:17]
	v_exp_f32_e32 v98, v98
	v_exp_f32_e32 v99, v99
	v_exp_f32_e32 v100, v100
	v_exp_f32_e32 v101, v101
	s_waitcnt lgkmcnt(12)
	v_mfma_f32_32x32x16_f16 v[18:33], v[158:161], v[174:177], v[18:33]
	v_exp_f32_e32 v102, v102
	v_exp_f32_e32 v103, v103
	v_exp_f32_e32 v104, v104
	v_exp_f32_e32 v105, v105
	ds_read_b128 v[58:61], v211
	ds_read_b128 v[114:117], v211 offset:4096
	s_waitcnt lgkmcnt(12)
	v_mfma_f32_32x32x16_f16 v[2:17], v[150:153], v[170:173], v[2:17]
	v_exp_f32_e32 v106, v106
	v_exp_f32_e32 v107, v107
	v_exp_f32_e32 v108, v108
	v_exp_f32_e32 v109, v109
	ds_read_b128 v[182:185], v210
	ds_read_b128 v[174:177], v210 offset:4096
	s_waitcnt lgkmcnt(12)
	v_mfma_f32_32x32x16_f16 v[18:33], v[150:153], v[74:77], v[18:33]
	v_exp_f32_e32 v110, v110
	v_exp_f32_e32 v111, v111
	v_exp_f32_e32 v112, v112
	v_exp_f32_e32 v113, v113
	ds_read_b128 v[178:181], v209
	ds_read_b128 v[166:169], v209 offset:4096
	s_waitcnt lgkmcnt(12)
	v_mfma_f32_32x32x16_f16 v[2:17], v[142:145], v[70:73], v[2:17]
	v_exp_f32_e32 v82, v82
	v_exp_f32_e32 v83, v83
	v_exp_f32_e32 v84, v84
	v_exp_f32_e32 v85, v85
	ds_read_b128 v[170:173], v208
	ds_read_b128 v[162:165], v208 offset:4096
	s_waitcnt lgkmcnt(12)
	v_mfma_f32_32x32x16_f16 v[18:33], v[142:145], v[66:69], v[18:33]
	v_exp_f32_e32 v86, v86
	v_exp_f32_e32 v87, v87
	v_exp_f32_e32 v88, v88
	v_exp_f32_e32 v89, v89
	s_waitcnt lgkmcnt(10)
	v_mfma_f32_32x32x16_f16 v[2:17], v[130:133], v[54:57], v[2:17]
	v_exp_f32_e32 v90, v90
	v_exp_f32_e32 v91, v91
	v_exp_f32_e32 v92, v92
	v_exp_f32_e32 v93, v93
	s_waitcnt lgkmcnt(8)
	v_mfma_f32_32x32x16_f16 v[18:33], v[130:133], v[50:53], v[18:33]
	v_exp_f32_e32 v94, v94
	v_exp_f32_e32 v95, v95
	v_exp_f32_e32 v96, v96
	v_exp_f32_e32 v97, v97
	s_waitcnt vmcnt(2) lgkmcnt(0)
	s_barrier
	s_andn2_b64 vcc, exec, s[26:27]
	s_cbranch_vccnz .Lu2_4
	s_waitcnt lgkmcnt(0)
	v_add_u32_e32 v66, s38, v212
	ds_read_b128 v[50:53], v66 offset:49248
	ds_read_b128 v[54:57], v66 offset:49216
	ds_read_b128 v[62:65], v66 offset:49184
	ds_read_b128 v[66:69], v66 offset:49152
	s_waitcnt lgkmcnt(3)
	v_pk_mul_f32 v[14:15], v[14:15], v[50:51]
	s_waitcnt lgkmcnt(2)
	v_pk_mul_f32 v[10:11], v[10:11], v[54:55]
	s_waitcnt lgkmcnt(1)
	v_pk_mul_f32 v[6:7], v[6:7], v[62:63]
	v_pk_mul_f32 v[16:17], v[16:17], v[52:53]
	v_pk_mul_f32 v[12:13], v[12:13], v[56:57]
	v_pk_mul_f32 v[8:9], v[8:9], v[64:65]
	s_waitcnt lgkmcnt(0)
	v_pk_mul_f32 v[4:5], v[4:5], v[68:69]
	v_pk_mul_f32 v[2:3], v[2:3], v[66:67]
	v_pk_mul_f32 v[30:31], v[30:31], v[50:51]
	v_pk_mul_f32 v[26:27], v[26:27], v[54:55]
	v_pk_mul_f32 v[22:23], v[22:23], v[62:63]
	v_pk_mul_f32 v[32:33], v[32:33], v[52:53]
	v_pk_mul_f32 v[28:29], v[28:29], v[56:57]
	v_pk_mul_f32 v[24:25], v[24:25], v[64:65]
	v_pk_mul_f32 v[20:21], v[20:21], v[68:69]
	v_pk_mul_f32 v[18:19], v[18:19], v[66:67]
.Lu2_4:
	s_add_i32 s26, s39, 0x2000
	s_cmpk_lg_i32 s39, 0x4000
	s_cselect_b32 s43, s26, 0
	ds_read_b64_tr_b16 v[126:127], v206 offset:40960
	ds_read_b64_tr_b16 v[128:129], v206 offset:41984
	s_waitcnt lgkmcnt(9)
	v_mfma_f32_32x32x16_f16 v[66:81], v[58:61], v[154:157], v[34:49]
	v_add_f32_e32 v224, v98, v102
	v_add_f32_e32 v225, v99, v103
	v_add_f32_e32 v226, v100, v104
	v_add_f32_e32 v227, v101, v105
	v_cvt_pk_f16_f32 v158, v98, v99
	v_cvt_pk_f16_f32 v159, v100, v101
	ds_read_b64_tr_b16 v[122:123], v207 offset:40960
	ds_read_b64_tr_b16 v[124:125], v207 offset:41984
	s_waitcnt lgkmcnt(10)
	v_mfma_f32_32x32x16_f16 v[50:65], v[114:117], v[154:157], v[34:49]
	v_add_f32_e32 v224, v106, v224
	v_add_f32_e32 v225, v107, v225
	v_add_f32_e32 v226, v108, v226
	v_add_f32_e32 v227, v109, v227
	v_cvt_pk_f16_f32 v160, v102, v103
	v_cvt_pk_f16_f32 v161, v104, v105
	ds_read_b64_tr_b16 v[118:119], v206 offset:43008
	ds_read_b64_tr_b16 v[120:121], v206 offset:44032
	s_waitcnt lgkmcnt(11)
	v_mfma_f32_32x32x16_f16 v[66:81], v[182:185], v[146:149], v[66:81]
	v_add_f32_e32 v224, v110, v224
	v_add_f32_e32 v225, v111, v225
	v_add_f32_e32 v226, v112, v226
	v_add_f32_e32 v227, v113, v227
	v_cvt_pk_f16_f32 v150, v106, v107
	v_cvt_pk_f16_f32 v151, v108, v109
	ds_read_b64_tr_b16 v[114:115], v207 offset:43008
	ds_read_b64_tr_b16 v[116:117], v207 offset:44032
	s_waitcnt lgkmcnt(12)
	v_mfma_f32_32x32x16_f16 v[50:65], v[174:177], v[146:149], v[50:65]
	v_add_f32_e32 v224, v82, v224
	v_add_f32_e32 v225, v83, v225
	v_add_f32_e32 v226, v84, v226
	v_add_f32_e32 v227, v85, v227
	v_cvt_pk_f16_f32 v152, v110, v111
	v_cvt_pk_f16_f32 v153, v112, v113
	ds_read_b64_tr_b16 v[106:107], v206 offset:45056
	ds_read_b64_tr_b16 v[108:109], v206 offset:46080
	s_waitcnt lgkmcnt(13)
	v_mfma_f32_32x32x16_f16 v[66:81], v[178:181], v[138:141], v[66:81]
	v_add_f32_e32 v224, v86, v224
	v_add_f32_e32 v225, v87, v225
	v_add_f32_e32 v226, v88, v226
	v_add_f32_e32 v227, v89, v227
	v_cvt_pk_f16_f32 v142, v82, v83
	v_cvt_pk_f16_f32 v143, v84, v85
	ds_read_b64_tr_b16 v[102:103], v207 offset:45056
	ds_read_b64_tr_b16 v[104:105], v207 offset:46080
	s_waitcnt lgkmcnt(14)
	v_mfma_f32_32x32x16_f16 v[50:65], v[166:169], v[138:141], v[50:65]
	v_add_f32_e32 v224, v90, v224
	v_add_f32_e32 v225, v91, v225
	v_add_f32_e32 v226, v92, v226
	v_add_f32_e32 v227, v93, v227
	v_cvt_pk_f16_f32 v144, v86, v87
	v_cvt_pk_f16_f32 v145, v88, v89
	ds_read_b64_tr_b16 v[98:99], v206 offset:47104
	ds_read_b64_tr_b16 v[100:101], v206 offset:48128
	s_waitcnt lgkmcnt(14)
	v_mfma_f32_32x32x16_f16 v[66:81], v[170:173], v[134:137], v[66:81]
	v_add_f32_e32 v224, v94, v224
	v_add_f32_e32 v225, v95, v225
	v_add_f32_e32 v226, v96, v226
	v_add_f32_e32 v227, v97, v227
	v_cvt_pk_f16_f32 v130, v90, v91
	v_cvt_pk_f16_f32 v131, v92, v93
	ds_read_b64_tr_b16 v[86:87], v207 offset:47104
	ds_read_b64_tr_b16 v[88:89], v207 offset:48128
	v_mfma_f32_32x32x16_f16 v[50:65], v[162:165], v[134:137], v[50:65]
	v_add_f32_e32 v224, v224, v225
	v_add_f32_e32 v226, v226, v227
	v_add_f32_e32 v84, v224, v226
	v_cvt_pk_f16_f32 v132, v94, v95
	v_cvt_pk_f16_f32 v133, v96, v97
	s_setprio 1
	s_add_u32 s54, s50, 0x2000
	s_addc_u32 s55, s51, 0
	s_add_i32 s26, s39, s36
	s_mov_b32 m0, s26
	s_nop 0
	global_load_lds_dwordx4 v221, s[54:55]
	v_max_f32_e32 v82, v66, v67
	s_nop 1
	v_max3_f32 v83, v68, v69, v51
	v_max3_f32 v82, v82, v50, v52
	v_max3_f32 v82, v82, v53, v70
	v_max3_f32 v83, v83, v72, v73
	v_max3_f32 v82, v82, v71, v54
	v_max3_f32 v83, v83, v56, v57
	v_max3_f32 v82, v82, v55, v74
	v_max3_f32 v83, v83, v76, v77
	v_max3_f32 v82, v82, v75, v58
	v_max3_f32 v83, v83, v60, v61
	v_max3_f32 v82, v82, v59, v78
	v_max3_f32 v83, v83, v80, v81
	v_max3_f32 v82, v82, v79, v62
	v_max3_f32 v83, v83, v64, v65
	v_max3_f32 v82, v82, v63, v83
	v_add_f32_e32 v183, v198, v84
	s_add_u32 s54, s52, 0x2000
	s_addc_u32 s55, s53, 0
	s_add_i32 s26, s43, s35
	s_mov_b32 m0, s26
	s_nop 0
	global_load_lds_dwordx4 v222, s[54:55]
	v_cmp_lt_f32_e32 vcc, s41, v82
	s_cmp_lg_u64 vcc, 0
	s_cselect_b64 s[26:27], -1, 0
	s_cbranch_vccnz .Lu2_12
.Lu2_5:
	s_setprio 0
	s_waitcnt lgkmcnt(14)
	v_mfma_f32_32x32x16_f16 v[2:17], v[158:161], v[126:129], v[2:17]
	v_exp_f32_e32 v66, v66
	v_exp_f32_e32 v67, v67
	v_exp_f32_e32 v68, v68
	v_exp_f32_e32 v69, v69
	s_waitcnt lgkmcnt(12)
	v_mfma_f32_32x32x16_f16 v[18:33], v[158:161], v[122:125], v[18:33]
	v_exp_f32_e32 v70, v70
	v_exp_f32_e32 v71, v71
	v_exp_f32_e32 v72, v72
	v_exp_f32_e32 v73, v73
	ds_read_b128 v[82:85], v211 offset:8192
	ds_read_b128 v[170:173], v211 offset:12288
	s_waitcnt lgkmcnt(12)
	v_mfma_f32_32x32x16_f16 v[2:17], v[150:153], v[118:121], v[2:17]
	v_exp_f32_e32 v74, v74
	v_exp_f32_e32 v75, v75
	v_exp_f32_e32 v76, v76
	v_exp_f32_e32 v77, v77
	ds_read_b128 v[166:169], v210 offset:8192
	ds_read_b128 v[162:165], v210 offset:12288
	s_waitcnt lgkmcnt(12)
	v_mfma_f32_32x32x16_f16 v[18:33], v[150:153], v[114:117], v[18:33]
	v_exp_f32_e32 v78, v78
	v_exp_f32_e32 v79, v79
	v_exp_f32_e32 v80, v80
	v_exp_f32_e32 v81, v81
	ds_read_b128 v[126:129], v209 offset:8192
	ds_read_b128 v[122:125], v209 offset:12288
	s_waitcnt lgkmcnt(12)
	v_mfma_f32_32x32x16_f16 v[2:17], v[142:145], v[106:109], v[2:17]
	v_exp_f32_e32 v50, v50
	v_exp_f32_e32 v51, v51
	v_exp_f32_e32 v52, v52
	v_exp_f32_e32 v53, v53
	ds_read_b128 v[118:121], v208 offset:8192
	ds_read_b128 v[114:117], v208 offset:12288
	s_waitcnt lgkmcnt(12)
	v_mfma_f32_32x32x16_f16 v[18:33], v[142:145], v[102:105], v[18:33]
	v_exp_f32_e32 v54, v54
	v_exp_f32_e32 v55, v55
	v_exp_f32_e32 v56, v56
	v_exp_f32_e32 v57, v57
	s_waitcnt lgkmcnt(10)
	v_mfma_f32_32x32x16_f16 v[2:17], v[130:133], v[98:101], v[2:17]
	v_exp_f32_e32 v58, v58
	v_exp_f32_e32 v59, v59
	v_exp_f32_e32 v60, v60
	v_exp_f32_e32 v61, v61
	s_waitcnt lgkmcnt(8)
	v_mfma_f32_32x32x16_f16 v[18:33], v[130:133], v[86:89], v[18:33]
	v_exp_f32_e32 v62, v62
	v_exp_f32_e32 v63, v63
	v_exp_f32_e32 v64, v64
	v_exp_f32_e32 v65, v65
	s_waitcnt vmcnt(2) lgkmcnt(0)
	s_barrier
	s_andn2_b64 vcc, exec, s[26:27]
	s_cbranch_vccnz .Lu2_7
	s_waitcnt lgkmcnt(0)
	v_add_u32_e32 v98, s38, v212
	ds_read_b128 v[86:89], v98 offset:49248
	ds_read_b128 v[90:93], v98 offset:49216
	ds_read_b128 v[94:97], v98 offset:49152
	ds_read_b128 v[98:101], v98 offset:49184
	s_waitcnt lgkmcnt(3)
	v_pk_mul_f32 v[16:17], v[16:17], v[88:89]
	v_pk_mul_f32 v[14:15], v[14:15], v[86:87]
	s_waitcnt lgkmcnt(2)
	v_pk_mul_f32 v[12:13], v[12:13], v[92:93]
	v_pk_mul_f32 v[10:11], v[10:11], v[90:91]
	s_waitcnt lgkmcnt(0)
	v_pk_mul_f32 v[8:9], v[8:9], v[100:101]
	v_pk_mul_f32 v[6:7], v[6:7], v[98:99]
	v_pk_mul_f32 v[4:5], v[4:5], v[96:97]
	v_pk_mul_f32 v[2:3], v[2:3], v[94:95]
	v_pk_mul_f32 v[32:33], v[32:33], v[88:89]
	v_pk_mul_f32 v[30:31], v[30:31], v[86:87]
	v_pk_mul_f32 v[28:29], v[28:29], v[92:93]
	v_pk_mul_f32 v[26:27], v[26:27], v[90:91]
	v_pk_mul_f32 v[24:25], v[24:25], v[100:101]
	v_pk_mul_f32 v[22:23], v[22:23], v[98:99]
	v_pk_mul_f32 v[20:21], v[20:21], v[96:97]
	v_pk_mul_f32 v[18:19], v[18:19], v[94:95]
